# PTK top-k: next chunk's 32 score loads prefetched during the current chunk's sorting network (plus RTO/rtp load batching)
# speedup vs baseline: 1.0041x; 1.0031x over previous
.LBB0_1700:
	s_getreg_b32 s2, hwreg(HW_REG_HW_ID, 0, 6)
	s_and_b32 s2, s2, 63
	s_lshl_b32 s2, s2, 2
	s_add_i32 s2, s2, 0
	s_add_i32 s2, s2, 0x20010
	v_mov_b32_e32 v4, s2
	ds_read_b32 v37, v4
	v_ashrrev_i32_e32 v4, 3, v44
	v_add_u32_e32 v4, v4, v45
	v_ashrrev_i32_e32 v5, 31, v4
	v_mbcnt_lo_u32_b32 v36, -1, 0
	v_mbcnt_hi_u32_b32 v36, -1, v36
	v_lshlrev_b64 v[4:5], 16, v[4:5]
	v_and_b32_e32 v46, 63, v36
	v_lshl_or_b32 v4, v46, 2, v4
	v_lshl_add_u64 v[4:5], s[6:7], 0, v[4:5]
	s_mov_b32 s2, -16
	s_mov_b32 s10, 0
	v_add_co_u32_e32 v134, vcc, 0xffff8000, v4
	s_nop 1
	v_addc_co_u32_e32 v135, vcc, -1, v5, vcc
	global_load_dword v100, v[134:135], off offset:-3840
	global_load_dword v101, v[4:5], off offset:-3840
	global_load_dword v102, v[134:135], off offset:-3584
	global_load_dword v103, v[4:5], off offset:-3584
	global_load_dword v104, v[134:135], off offset:-3328
	global_load_dword v105, v[4:5], off offset:-3328
	global_load_dword v106, v[134:135], off offset:-3072
	global_load_dword v107, v[4:5], off offset:-3072
	global_load_dword v108, v[134:135], off offset:-2816
	global_load_dword v109, v[4:5], off offset:-2816
	global_load_dword v110, v[134:135], off offset:-2560
	global_load_dword v111, v[4:5], off offset:-2560
	global_load_dword v112, v[134:135], off offset:-2304
	global_load_dword v113, v[4:5], off offset:-2304
	global_load_dword v114, v[134:135], off offset:-2048
	global_load_dword v115, v[4:5], off offset:-2048
	global_load_dword v116, v[134:135], off offset:-1792
	global_load_dword v117, v[4:5], off offset:-1792
	global_load_dword v118, v[134:135], off offset:-1536
	global_load_dword v119, v[4:5], off offset:-1536
	global_load_dword v120, v[134:135], off offset:-1280
	global_load_dword v121, v[4:5], off offset:-1280
	global_load_dword v122, v[134:135], off offset:-1024
	global_load_dword v123, v[4:5], off offset:-1024
	global_load_dword v124, v[134:135], off offset:-768
	global_load_dword v125, v[4:5], off offset:-768
	global_load_dword v126, v[134:135], off offset:-512
	global_load_dword v127, v[4:5], off offset:-512
	global_load_dword v128, v[134:135], off offset:-256
	global_load_dword v129, v[4:5], off offset:-256
	global_load_dword v130, v[134:135], off
	global_load_dword v131, v[4:5], off
.LBB0_1701:
	s_movk_i32 s11, 0x8000
	v_add_co_u32_e32 v6, vcc, s11, v4
	s_cmp_eq_u32 s10, 0
	s_nop 0
	v_addc_co_u32_e32 v7, vcc, -1, v5, vcc
	s_waitcnt vmcnt(0)
	v_mov_b32_e32 v14, v100
	v_mov_b32_e32 v15, v101
	v_mov_b32_e32 v20, v102
	v_mov_b32_e32 v73, v103
	v_mov_b32_e32 v74, v104
	v_mov_b32_e32 v75, v105
	v_mov_b32_e32 v76, v106
	v_mov_b32_e32 v30, v107
	v_mov_b32_e32 v35, v108
	v_mov_b32_e32 v34, v109
	v_mov_b32_e32 v32, v110
	v_mov_b32_e32 v31, v111
	v_mov_b32_e32 v29, v112
	v_mov_b32_e32 v28, v113
	v_mov_b32_e32 v27, v114
	v_mov_b32_e32 v26, v115
	v_mov_b32_e32 v25, v116
	v_mov_b32_e32 v24, v117
	v_mov_b32_e32 v23, v118
	v_mov_b32_e32 v22, v119
	v_mov_b32_e32 v21, v120
	v_mov_b32_e32 v19, v121
	v_mov_b32_e32 v18, v122
	v_mov_b32_e32 v17, v123
	v_mov_b32_e32 v16, v124
	v_mov_b32_e32 v13, v125
	v_mov_b32_e32 v12, v126
	v_mov_b32_e32 v11, v127
	v_mov_b32_e32 v10, v128
	v_mov_b32_e32 v9, v129
	v_mov_b32_e32 v8, v130
	v_mov_b32_e32 v6, v131
	v_add_co_u32_e32 v132, vcc, 0x1000, v4
	s_nop 1
	v_addc_co_u32_e32 v133, vcc, 0, v5, vcc
	v_add_co_u32_e32 v134, vcc, 0xffff8000, v132
	s_nop 1
	v_addc_co_u32_e32 v135, vcc, -1, v133, vcc
	global_load_dword v100, v[134:135], off offset:-3840
	global_load_dword v101, v[132:133], off offset:-3840
	global_load_dword v102, v[134:135], off offset:-3584
	global_load_dword v103, v[132:133], off offset:-3584
	global_load_dword v104, v[134:135], off offset:-3328
	global_load_dword v105, v[132:133], off offset:-3328
	global_load_dword v106, v[134:135], off offset:-3072
	global_load_dword v107, v[132:133], off offset:-3072
	global_load_dword v108, v[134:135], off offset:-2816
	global_load_dword v109, v[132:133], off offset:-2816
	global_load_dword v110, v[134:135], off offset:-2560
	global_load_dword v111, v[132:133], off offset:-2560
	global_load_dword v112, v[134:135], off offset:-2304
	global_load_dword v113, v[132:133], off offset:-2304
	global_load_dword v114, v[134:135], off offset:-2048
	global_load_dword v115, v[132:133], off offset:-2048
	global_load_dword v116, v[134:135], off offset:-1792
	global_load_dword v117, v[132:133], off offset:-1792
	global_load_dword v118, v[134:135], off offset:-1536
	global_load_dword v119, v[132:133], off offset:-1536
	global_load_dword v120, v[134:135], off offset:-1280
	global_load_dword v121, v[132:133], off offset:-1280
	global_load_dword v122, v[134:135], off offset:-1024
	global_load_dword v123, v[132:133], off offset:-1024
	global_load_dword v124, v[134:135], off offset:-768
	global_load_dword v125, v[132:133], off offset:-768
	global_load_dword v126, v[134:135], off offset:-512
	global_load_dword v127, v[132:133], off offset:-512
	global_load_dword v128, v[134:135], off offset:-256
	global_load_dword v129, v[132:133], off offset:-256
	global_load_dword v130, v[134:135], off
	global_load_dword v131, v[132:133], off
	v_not_b32_e32 v7, v14
	v_or_b32_e32 v33, 0x80000000, v14
	v_cmp_gt_i32_e32 vcc, 0, v14
	v_not_b32_e32 v14, v15
	v_cndmask_b32_e32 v7, v33, v7, vcc
	v_or_b32_e32 v33, 0x80000000, v15
	v_cmp_gt_i32_e32 vcc, 0, v15
	v_not_b32_e32 v15, v20
	v_and_b32_e32 v7, 0xffffff80, v7
	v_cndmask_b32_e32 v14, v33, v14, vcc
	v_or_b32_e32 v33, 0x80000000, v20
	v_cmp_gt_i32_e32 vcc, 0, v20
	v_or_b32_e32 v20, 0x80000000, v73
	v_add_u32_e32 v7, s10, v7
	v_cndmask_b32_e32 v15, v33, v15, vcc
	v_and_b32_e32 v15, 0xffffff80, v15
	v_add_u32_e32 v15, s10, v15
	v_add_u32_e32 v33, 0x7e, v15
	v_not_b32_e32 v15, v73
	v_cmp_gt_i32_e32 vcc, 0, v73
	v_or_b32_e32 v73, 0x80000000, v74
	v_add_u32_e32 v7, 0x7f, v7
	v_cndmask_b32_e32 v15, v20, v15, vcc
	v_not_b32_e32 v20, v74
	v_cmp_gt_i32_e32 vcc, 0, v74
	v_or_b32_e32 v74, 0x80000000, v75
	v_and_b32_e32 v14, 0xffffff80, v14
	v_cndmask_b32_e32 v20, v73, v20, vcc
	v_and_b32_e32 v20, 0xffffff80, v20
	v_add_u32_e32 v20, s10, v20
	v_add_u32_e32 v73, 0x7d, v20
	v_not_b32_e32 v20, v75
	v_cmp_gt_i32_e32 vcc, 0, v75
	v_or_b32_e32 v75, 0x80000000, v76
	v_and_b32_e32 v15, 0xffffff80, v15
	v_cndmask_b32_e32 v20, v74, v20, vcc
	v_not_b32_e32 v74, v76
	v_cmp_gt_i32_e32 vcc, 0, v76
	v_or_b32_e32 v76, 0x80000000, v30
	v_and_b32_e32 v20, 0xffffff80, v20
	v_cndmask_b32_e32 v74, v75, v74, vcc
	v_not_b32_e32 v75, v30
	v_cmp_gt_i32_e32 vcc, 0, v30
	v_and_b32_e32 v74, 0xffffff80, v74
	v_add_u32_e32 v74, s10, v74
	v_cndmask_b32_e32 v30, v76, v75, vcc
	v_not_b32_e32 v75, v35
	v_or_b32_e32 v76, 0x80000000, v35
	v_cmp_gt_i32_e32 vcc, 0, v35
	v_add_u32_e32 v74, 0x7c, v74
	v_and_b32_e32 v30, 0xffffff80, v30
	v_cndmask_b32_e32 v35, v76, v75, vcc
	v_not_b32_e32 v75, v34
	v_or_b32_e32 v76, 0x80000000, v34
	v_cmp_gt_i32_e32 vcc, 0, v34
	v_and_b32_e32 v35, 0xffffff80, v35
	v_add_u32_e32 v35, s10, v35
	v_cndmask_b32_e32 v34, v76, v75, vcc
	v_not_b32_e32 v75, v32
	v_or_b32_e32 v76, 0x80000000, v32
	v_cmp_gt_i32_e32 vcc, 0, v32
	v_add_u32_e32 v35, 0x7b, v35
	v_and_b32_e32 v34, 0xffffff80, v34
	v_cndmask_b32_e32 v32, v76, v75, vcc
	v_not_b32_e32 v75, v31
	v_or_b32_e32 v76, 0x80000000, v31
	v_cmp_gt_i32_e32 vcc, 0, v31
	v_and_b32_e32 v32, 0xffffff80, v32
	v_add_u32_e32 v32, s10, v32
	v_cndmask_b32_e32 v31, v76, v75, vcc
	v_not_b32_e32 v75, v29
	v_or_b32_e32 v76, 0x80000000, v29
	v_cmp_gt_i32_e32 vcc, 0, v29
	v_add_u32_e32 v32, 0x7a, v32
	v_and_b32_e32 v31, 0xffffff80, v31
	v_cndmask_b32_e32 v29, v76, v75, vcc
	v_not_b32_e32 v75, v28
	v_or_b32_e32 v76, 0x80000000, v28
	v_cmp_gt_i32_e32 vcc, 0, v28
	v_and_b32_e32 v29, 0xffffff80, v29
	v_add_u32_e32 v29, s10, v29
	v_cndmask_b32_e32 v28, v76, v75, vcc
	v_not_b32_e32 v75, v27
	v_or_b32_e32 v76, 0x80000000, v27
	v_cmp_gt_i32_e32 vcc, 0, v27
	v_add_u32_e32 v29, 0x79, v29
	v_and_b32_e32 v28, 0xffffff80, v28
	v_cndmask_b32_e32 v27, v76, v75, vcc
	v_not_b32_e32 v75, v26
	v_or_b32_e32 v76, 0x80000000, v26
	v_cmp_gt_i32_e32 vcc, 0, v26
	v_and_b32_e32 v27, 0xffffff80, v27
	v_add_u32_e32 v27, s10, v27
	v_cndmask_b32_e32 v26, v76, v75, vcc
	v_not_b32_e32 v75, v25
	v_or_b32_e32 v76, 0x80000000, v25
	v_cmp_gt_i32_e32 vcc, 0, v25
	v_add_u32_e32 v27, 0x78, v27
	v_and_b32_e32 v26, 0xffffff80, v26
	v_cndmask_b32_e32 v25, v76, v75, vcc
	v_not_b32_e32 v75, v24
	v_or_b32_e32 v76, 0x80000000, v24
	v_cmp_gt_i32_e32 vcc, 0, v24
	v_and_b32_e32 v25, 0xffffff80, v25
	v_add_u32_e32 v25, s10, v25
	v_cndmask_b32_e32 v24, v76, v75, vcc
	v_not_b32_e32 v75, v23
	v_or_b32_e32 v76, 0x80000000, v23
	v_cmp_gt_i32_e32 vcc, 0, v23
	v_add_u32_e32 v25, 0x77, v25
	v_and_b32_e32 v24, 0xffffff80, v24
	v_cndmask_b32_e32 v23, v76, v75, vcc
	v_not_b32_e32 v75, v22
	v_or_b32_e32 v76, 0x80000000, v22
	v_cmp_gt_i32_e32 vcc, 0, v22
	v_and_b32_e32 v23, 0xffffff80, v23
	v_add_u32_e32 v23, s10, v23
	v_cndmask_b32_e32 v22, v76, v75, vcc
	v_not_b32_e32 v75, v21
	v_or_b32_e32 v76, 0x80000000, v21
	v_cmp_gt_i32_e32 vcc, 0, v21
	v_add_u32_e32 v23, 0x76, v23
	v_and_b32_e32 v22, 0xffffff80, v22
	v_cndmask_b32_e32 v21, v76, v75, vcc
	v_not_b32_e32 v75, v19
	v_or_b32_e32 v76, 0x80000000, v19
	v_cmp_gt_i32_e32 vcc, 0, v19
	v_and_b32_e32 v21, 0xffffff80, v21
	v_add_u32_e32 v21, s10, v21
	v_cndmask_b32_e32 v19, v76, v75, vcc
	v_and_b32_e32 v19, 0xffffff80, v19
	v_add_u32_e32 v19, s10, v19
	v_add_u32_e32 v75, 0x75, v19
	v_not_b32_e32 v19, v18
	v_or_b32_e32 v76, 0x80000000, v18
	v_cmp_gt_i32_e32 vcc, 0, v18
	v_add_u32_e32 v21, 0x75, v21
	v_add_u32_e32 v14, s10, v14
	v_cndmask_b32_e32 v18, v76, v19, vcc
	v_not_b32_e32 v19, v17
	v_or_b32_e32 v76, 0x80000000, v17
	v_cmp_gt_i32_e32 vcc, 0, v17
	v_and_b32_e32 v18, 0xffffff80, v18
	v_add_u32_e32 v18, s10, v18
	v_cndmask_b32_e32 v17, v76, v19, vcc
	v_and_b32_e32 v17, 0xffffff80, v17
	v_add_u32_e32 v17, s10, v17
	v_add_u32_e32 v76, 0x74, v17
	v_not_b32_e32 v17, v16
	v_or_b32_e32 v19, 0x80000000, v16
	v_cmp_gt_i32_e32 vcc, 0, v16
	v_add_u32_e32 v18, 0x74, v18
	v_add_u32_e32 v15, s10, v15
	v_cndmask_b32_e32 v16, v19, v17, vcc
	v_not_b32_e32 v17, v13
	v_or_b32_e32 v19, 0x80000000, v13
	v_cmp_gt_i32_e32 vcc, 0, v13
	v_and_b32_e32 v16, 0xffffff80, v16
	v_add_u32_e32 v16, s10, v16
	v_cndmask_b32_e32 v13, v19, v17, vcc
	v_and_b32_e32 v13, 0xffffff80, v13
	v_add_u32_e32 v13, s10, v13
	v_add_u32_e32 v77, 0x73, v13
	v_not_b32_e32 v13, v12
	v_or_b32_e32 v17, 0x80000000, v12
	v_cmp_gt_i32_e32 vcc, 0, v12
	v_add_u32_e32 v16, 0x73, v16
	v_max_u32_e32 v19, v27, v29
	v_cndmask_b32_e32 v12, v17, v13, vcc
	v_not_b32_e32 v13, v11
	v_or_b32_e32 v17, 0x80000000, v11
	v_cmp_gt_i32_e32 vcc, 0, v11
	v_and_b32_e32 v12, 0xffffff80, v12
	v_add_u32_e32 v12, s10, v12
	v_cndmask_b32_e32 v11, v17, v13, vcc
	v_and_b32_e32 v11, 0xffffff80, v11
	v_add_u32_e32 v11, s10, v11
	v_add_u32_e32 v78, 0x72, v11
	v_not_b32_e32 v11, v10
	v_or_b32_e32 v13, 0x80000000, v10
	v_cmp_gt_i32_e32 vcc, 0, v10
	v_add_u32_e32 v12, 0x72, v12
	v_min_u32_e32 v17, v35, v32
	v_cndmask_b32_e32 v10, v13, v11, vcc
	v_not_b32_e32 v11, v9
	v_or_b32_e32 v13, 0x80000000, v9
	v_cmp_gt_i32_e32 vcc, 0, v9
	v_and_b32_e32 v10, 0xffffff80, v10
	v_add_u32_e32 v10, s10, v10
	v_cndmask_b32_e32 v9, v13, v11, vcc
	v_and_b32_e32 v9, 0xffffff80, v9
	v_add_u32_e32 v9, s10, v9
	v_add_u32_e32 v79, 0x71, v9
	v_not_b32_e32 v9, v8
	v_or_b32_e32 v11, 0x80000000, v8
	v_cmp_gt_i32_e32 vcc, 0, v8
	v_add_u32_e32 v10, 0x71, v10
	v_max_u32_e32 v13, v35, v32
	v_cndmask_b32_e32 v8, v11, v9, vcc
	v_not_b32_e32 v9, v6
	v_or_b32_e32 v11, 0x80000000, v6
	v_cmp_gt_i32_e32 vcc, 0, v6
	v_and_b32_e32 v8, 0xffffff80, v8
	v_add_u32_e32 v8, s10, v8
	v_cndmask_b32_e32 v6, v11, v9, vcc
	v_and_b32_e32 v6, 0xffffff80, v6
	v_add_u32_e32 v8, 0x70, v8
	v_add_u32_e32 v6, s10, v6
	v_add_u32_e32 v80, 0x70, v6
	v_max_u32_e32 v6, v7, v33
	v_min_u32_e32 v7, v7, v33
	v_max_u32_e32 v9, v74, v73
	v_min_u32_e32 v11, v74, v73
	v_min_u32_e32 v27, v27, v29
	v_max_u32_e32 v29, v25, v23
	v_min_u32_e32 v23, v25, v23
	v_max_u32_e32 v25, v18, v21
	v_min_u32_e32 v18, v18, v21
	v_max_u32_e32 v21, v16, v12
	v_min_u32_e32 v12, v16, v12
	v_max_u32_e32 v16, v8, v10
	v_min_u32_e32 v8, v8, v10
	v_max_u32_e32 v10, v6, v11
	v_min_u32_e32 v6, v6, v11
	v_max_u32_e32 v11, v7, v9
	v_min_u32_e32 v7, v7, v9
	v_max_u32_e32 v9, v27, v13
	v_min_u32_e32 v13, v27, v13
	v_max_u32_e32 v27, v19, v17
	v_min_u32_e32 v17, v19, v17
	v_max_u32_e32 v19, v29, v18
	v_min_u32_e32 v18, v29, v18
	v_max_u32_e32 v29, v23, v25
	v_min_u32_e32 v23, v23, v25
	v_max_u32_e32 v25, v8, v21
	v_min_u32_e32 v8, v8, v21
	v_max_u32_e32 v21, v16, v12
	v_min_u32_e32 v12, v16, v12
	v_max_u32_e32 v16, v10, v11
	v_min_u32_e32 v10, v10, v11
	v_max_u32_e32 v11, v6, v7
	v_min_u32_e32 v6, v6, v7
	v_max_u32_e32 v7, v17, v13
	v_min_u32_e32 v13, v17, v13
	v_max_u32_e32 v17, v27, v9
	v_min_u32_e32 v9, v27, v9
	v_max_u32_e32 v27, v19, v29
	v_min_u32_e32 v19, v19, v29
	v_max_u32_e32 v29, v18, v23
	v_min_u32_e32 v18, v18, v23
	v_max_u32_e32 v23, v12, v8
	v_min_u32_e32 v8, v12, v8
	v_max_u32_e32 v12, v21, v25
	v_min_u32_e32 v21, v21, v25
	v_max_u32_e32 v25, v16, v13
	v_min_u32_e32 v13, v16, v13
	v_max_u32_e32 v16, v10, v7
	v_min_u32_e32 v7, v10, v7
	v_max_u32_e32 v10, v11, v9
	v_min_u32_e32 v9, v11, v9
	v_max_u32_e32 v11, v6, v17
	v_min_u32_e32 v6, v6, v17
	v_max_u32_e32 v17, v8, v27
	v_min_u32_e32 v8, v8, v27
	v_max_u32_e32 v27, v23, v19
	v_min_u32_e32 v19, v23, v19
	v_max_u32_e32 v23, v21, v29
	v_min_u32_e32 v21, v21, v29
	v_max_u32_e32 v29, v12, v18
	v_min_u32_e32 v12, v12, v18
	v_max_u32_e32 v18, v25, v10
	v_min_u32_e32 v10, v25, v10
	v_max_u32_e32 v25, v16, v11
	v_min_u32_e32 v11, v16, v11
	v_max_u32_e32 v16, v13, v9
	v_min_u32_e32 v9, v13, v9
	v_max_u32_e32 v13, v7, v6
	v_min_u32_e32 v6, v7, v6
	v_max_u32_e32 v7, v21, v8
	v_min_u32_e32 v8, v21, v8
	v_max_u32_e32 v21, v12, v19
	v_min_u32_e32 v12, v12, v19
	v_max_u32_e32 v19, v23, v17
	v_min_u32_e32 v17, v23, v17
	v_max_u32_e32 v23, v29, v27
	v_min_u32_e32 v27, v29, v27
	v_max_u32_e32 v29, v18, v25
	v_min_u32_e32 v18, v18, v25
	v_max_u32_e32 v25, v10, v11
	v_min_u32_e32 v10, v10, v11
	v_max_u32_e32 v11, v16, v13
	v_min_u32_e32 v13, v16, v13
	v_max_u32_e32 v16, v9, v6
	v_min_u32_e32 v6, v9, v6
	v_max_u32_e32 v9, v12, v8
	v_min_u32_e32 v8, v12, v8
	v_max_u32_e32 v12, v21, v7
	v_min_u32_e32 v7, v21, v7
	v_max_u32_e32 v21, v27, v17
	v_min_u32_e32 v17, v27, v17
	v_max_u32_e32 v27, v23, v19
	v_min_u32_e32 v19, v23, v19
	v_max_u32_e32 v23, v29, v8
	v_min_u32_e32 v8, v29, v8
	v_max_u32_e32 v29, v18, v9
	v_min_u32_e32 v9, v18, v9
	v_max_u32_e32 v18, v25, v7
	v_min_u32_e32 v7, v25, v7
	v_max_u32_e32 v25, v10, v12
	v_min_u32_e32 v10, v10, v12
	v_max_u32_e32 v12, v11, v17
	v_min_u32_e32 v11, v11, v17
	v_max_u32_e32 v17, v13, v21
	v_min_u32_e32 v13, v13, v21
	v_max_u32_e32 v21, v16, v19
	v_min_u32_e32 v16, v16, v19
	v_max_u32_e32 v19, v6, v27
	v_min_u32_e32 v6, v6, v27
	v_add_u32_e32 v20, s10, v20
	v_add_u32_e32 v30, s10, v30
	v_add_u32_e32 v34, s10, v34
	v_add_u32_e32 v31, s10, v31
	v_add_u32_e32 v28, s10, v28
	v_add_u32_e32 v26, s10, v26
	v_add_u32_e32 v24, s10, v24
	v_add_u32_e32 v22, s10, v22
	v_max_u32_e32 v27, v23, v12
	v_min_u32_e32 v12, v23, v12
	v_max_u32_e32 v23, v29, v17
	v_min_u32_e32 v17, v29, v17
	v_max_u32_e32 v29, v18, v21
	v_min_u32_e32 v18, v18, v21
	v_max_u32_e32 v21, v25, v19
	v_min_u32_e32 v19, v25, v19
	v_max_u32_e32 v25, v8, v11
	v_min_u32_e32 v8, v8, v11
	v_max_u32_e32 v11, v9, v13
	v_min_u32_e32 v9, v9, v13
	v_max_u32_e32 v13, v7, v16
	v_min_u32_e32 v7, v7, v16
	v_max_u32_e32 v16, v10, v6
	v_min_u32_e32 v6, v10, v6
	v_add_u32_e32 v14, 0x7f, v14
	v_add_u32_e32 v15, 0x7e, v15
	v_add_u32_e32 v20, 0x7d, v20
	v_add_u32_e32 v30, 0x7c, v30
	v_add_u32_e32 v34, 0x7b, v34
	v_add_u32_e32 v31, 0x7a, v31
	v_add_u32_e32 v28, 0x79, v28
	v_add_u32_e32 v26, 0x78, v26
	v_add_u32_e32 v24, 0x77, v24
	v_add_u32_e32 v22, 0x76, v22
	v_max_u32_e32 v10, v27, v29
	v_min_u32_e32 v27, v27, v29
	v_max_u32_e32 v29, v23, v21
	v_min_u32_e32 v32, v23, v21
	v_max_u32_e32 v33, v12, v18
	v_min_u32_e32 v12, v12, v18
	v_max_u32_e32 v18, v17, v19
	v_min_u32_e32 v17, v17, v19
	v_max_u32_e32 v35, v25, v13
	v_min_u32_e32 v25, v25, v13
	v_max_u32_e32 v13, v11, v16
	v_min_u32_e32 v11, v11, v16
	v_max_u32_e32 v73, v8, v7
	v_min_u32_e32 v74, v8, v7
	v_max_u32_e32 v8, v9, v6
	v_min_u32_e32 v81, v9, v6
	v_max_u32_e32 v23, v10, v29
	v_min_u32_e32 v29, v10, v29
	v_max_u32_e32 v21, v27, v32
	v_min_u32_e32 v19, v27, v32
	v_max_u32_e32 v7, v33, v18
	v_min_u32_e32 v6, v33, v18
	v_max_u32_e32 v33, v12, v17
	v_min_u32_e32 v17, v12, v17
	v_max_u32_e32 v16, v35, v13
	v_min_u32_e32 v13, v35, v13
	v_max_u32_e32 v12, v25, v11
	v_min_u32_e32 v11, v25, v11
	v_max_u32_e32 v10, v73, v8
	v_min_u32_e32 v9, v73, v8
	v_max_u32_e32 v8, v74, v81
	v_min_u32_e32 v25, v74, v81
	v_max_u32_e32 v18, v14, v15
	v_min_u32_e32 v14, v14, v15
	v_max_u32_e32 v15, v30, v20
	v_min_u32_e32 v20, v30, v20
	v_max_u32_e32 v27, v34, v31
	v_min_u32_e32 v30, v34, v31
	v_max_u32_e32 v31, v26, v28
	v_min_u32_e32 v26, v26, v28
	v_max_u32_e32 v28, v24, v22
	v_min_u32_e32 v22, v24, v22
	v_max_u32_e32 v24, v76, v75
	v_min_u32_e32 v32, v76, v75
	v_max_u32_e32 v34, v77, v78
	v_min_u32_e32 v35, v77, v78
	v_max_u32_e32 v73, v80, v79
	v_min_u32_e32 v74, v80, v79
	v_max_u32_e32 v75, v18, v20
	v_min_u32_e32 v18, v18, v20
	v_max_u32_e32 v20, v14, v15
	v_min_u32_e32 v14, v14, v15
	v_max_u32_e32 v15, v26, v27
	v_min_u32_e32 v26, v26, v27
	v_max_u32_e32 v27, v31, v30
	v_min_u32_e32 v30, v31, v30
	v_max_u32_e32 v31, v28, v32
	v_min_u32_e32 v28, v28, v32
	v_max_u32_e32 v32, v22, v24
	v_min_u32_e32 v22, v22, v24
	v_max_u32_e32 v24, v74, v34
	v_min_u32_e32 v34, v74, v34
	v_max_u32_e32 v74, v73, v35
	v_min_u32_e32 v35, v73, v35
	v_max_u32_e32 v73, v75, v20
	v_min_u32_e32 v20, v75, v20
	v_max_u32_e32 v75, v18, v14
	v_min_u32_e32 v14, v18, v14
	v_max_u32_e32 v18, v30, v26
	v_min_u32_e32 v26, v30, v26
	v_max_u32_e32 v30, v27, v15
	v_min_u32_e32 v15, v27, v15
	v_max_u32_e32 v27, v31, v32
	v_min_u32_e32 v31, v31, v32
	v_max_u32_e32 v32, v28, v22
	v_min_u32_e32 v22, v28, v22
	v_max_u32_e32 v28, v35, v34
	v_min_u32_e32 v34, v35, v34
	v_max_u32_e32 v35, v74, v24
	v_min_u32_e32 v24, v74, v24
	v_max_u32_e32 v74, v73, v26
	v_min_u32_e32 v26, v73, v26
	v_max_u32_e32 v73, v20, v18
	v_min_u32_e32 v18, v20, v18
	v_max_u32_e32 v20, v75, v15
	v_min_u32_e32 v15, v75, v15
	v_max_u32_e32 v75, v14, v30
	v_min_u32_e32 v14, v14, v30
	v_max_u32_e32 v30, v34, v27
	v_min_u32_e32 v27, v34, v27
	v_max_u32_e32 v34, v28, v31
	v_min_u32_e32 v28, v28, v31
	v_max_u32_e32 v31, v24, v32
	v_min_u32_e32 v24, v24, v32
	v_max_u32_e32 v32, v35, v22
	v_min_u32_e32 v22, v35, v22
	v_max_u32_e32 v35, v74, v20
	v_min_u32_e32 v20, v74, v20
	v_max_u32_e32 v74, v73, v75
	v_min_u32_e32 v73, v73, v75
	v_max_u32_e32 v75, v26, v15
	v_min_u32_e32 v15, v26, v15
	v_max_u32_e32 v26, v18, v14
	v_min_u32_e32 v14, v18, v14
	v_max_u32_e32 v18, v24, v27
	v_min_u32_e32 v24, v24, v27
	v_max_u32_e32 v27, v22, v28
	v_min_u32_e32 v22, v22, v28
	v_max_u32_e32 v28, v31, v30
	v_min_u32_e32 v30, v31, v30
	v_max_u32_e32 v31, v32, v34
	v_min_u32_e32 v32, v32, v34
	v_max_u32_e32 v34, v35, v74
	v_min_u32_e32 v35, v35, v74
	v_max_u32_e32 v74, v20, v73
	v_min_u32_e32 v20, v20, v73
	v_max_u32_e32 v73, v75, v26
	v_min_u32_e32 v26, v75, v26
	v_max_u32_e32 v75, v15, v14
	v_min_u32_e32 v14, v15, v14
	v_max_u32_e32 v15, v22, v24
	v_min_u32_e32 v22, v22, v24
	v_max_u32_e32 v24, v27, v18
	v_min_u32_e32 v18, v27, v18
	v_max_u32_e32 v27, v32, v30
	v_min_u32_e32 v30, v32, v30
	v_max_u32_e32 v32, v31, v28
	v_min_u32_e32 v28, v31, v28
	v_max_u32_e32 v31, v34, v22
	v_min_u32_e32 v22, v34, v22
	v_max_u32_e32 v34, v35, v15
	v_min_u32_e32 v15, v35, v15
	v_max_u32_e32 v35, v74, v18
	v_min_u32_e32 v18, v74, v18
	v_max_u32_e32 v74, v20, v24
	v_min_u32_e32 v20, v20, v24
	v_max_u32_e32 v24, v73, v30
	v_min_u32_e32 v30, v73, v30
	v_max_u32_e32 v73, v26, v27
	v_min_u32_e32 v26, v26, v27
	v_max_u32_e32 v27, v75, v28
	v_min_u32_e32 v28, v75, v28
	v_max_u32_e32 v75, v14, v32
	v_min_u32_e32 v14, v14, v32
	v_max_u32_e32 v32, v31, v24
	v_min_u32_e32 v24, v31, v24
	v_max_u32_e32 v31, v34, v73
	v_min_u32_e32 v34, v34, v73
	v_max_u32_e32 v73, v35, v27
	v_min_u32_e32 v27, v35, v27
	v_max_u32_e32 v35, v74, v75
	v_min_u32_e32 v74, v74, v75
	v_max_u32_e32 v75, v22, v30
	v_min_u32_e32 v22, v22, v30
	v_max_u32_e32 v30, v15, v26
	v_min_u32_e32 v15, v15, v26
	v_max_u32_e32 v26, v18, v28
	v_min_u32_e32 v18, v18, v28
	v_max_u32_e32 v28, v20, v14
	v_min_u32_e32 v14, v20, v14
	v_max_u32_e32 v20, v32, v73
	v_min_u32_e32 v32, v32, v73
	v_max_u32_e32 v73, v31, v35
	v_min_u32_e32 v31, v31, v35
	v_max_u32_e32 v35, v24, v27
	v_min_u32_e32 v24, v24, v27
	v_max_u32_e32 v27, v34, v74
	v_min_u32_e32 v74, v34, v74
	v_max_u32_e32 v76, v75, v26
	v_min_u32_e32 v75, v75, v26
	v_max_u32_e32 v26, v30, v28
	v_min_u32_e32 v30, v30, v28
	v_max_u32_e32 v77, v22, v18
	v_min_u32_e32 v78, v22, v18
	v_max_u32_e32 v22, v15, v14
	v_min_u32_e32 v79, v15, v14
	v_max_u32_e32 v28, v20, v73
	v_min_u32_e32 v34, v20, v73
	v_max_u32_e32 v18, v32, v31
	v_min_u32_e32 v20, v32, v31
	v_max_u32_e32 v15, v35, v27
	v_min_u32_e32 v14, v35, v27
	v_max_u32_e32 v32, v24, v74
	v_min_u32_e32 v74, v24, v74
	v_max_u32_e32 v35, v76, v26
	v_min_u32_e32 v26, v76, v26
	v_max_u32_e32 v31, v75, v30
	v_min_u32_e32 v24, v75, v30
	v_max_u32_e32 v27, v77, v22
	v_min_u32_e32 v22, v77, v22
	v_max_u32_e32 v73, v78, v79
	v_min_u32_e32 v30, v78, v79
	s_cbranch_scc1 .LBB0_1703
	v_max_u32_e32 v25, v57, v25
	v_max_u32_e32 v8, v58, v8
	v_max_u32_e32 v9, v59, v9
	v_max_u32_e32 v10, v60, v10
	v_max_u32_e32 v11, v61, v11
	v_max_u32_e32 v12, v62, v12
	v_max_u32_e32 v13, v63, v13
	v_max_u32_e32 v16, v64, v16
	v_max_u32_e32 v17, v65, v17
	v_max_u32_e32 v33, v66, v33
	v_max_u32_e32 v6, v67, v6
	v_max_u32_e32 v7, v68, v7
	v_max_u32_e32 v19, v69, v19
	v_max_u32_e32 v21, v70, v21
	v_max_u32_e32 v29, v71, v29
	v_max_u32_e32 v23, v72, v23
	v_max_u32_e32 v30, v38, v30
	v_max_u32_e32 v38, v39, v73
	v_max_u32_e32 v22, v40, v22
	v_max_u32_e32 v27, v41, v27
	v_max_u32_e32 v24, v42, v24
	v_max_u32_e32 v31, v43, v31
	v_max_u32_e32 v26, v47, v26
	v_max_u32_e32 v35, v48, v35
	v_max_u32_e32 v39, v49, v74
	v_max_u32_e32 v32, v50, v32
	v_max_u32_e32 v14, v51, v14
	v_max_u32_e32 v15, v52, v15
	v_max_u32_e32 v20, v53, v20
	v_max_u32_e32 v18, v54, v18
	v_max_u32_e32 v34, v55, v34
	v_max_u32_e32 v28, v56, v28
	v_max_u32_e32 v57, v25, v17
	v_min_u32_e32 v17, v25, v17
	v_max_u32_e32 v25, v8, v33
	v_min_u32_e32 v8, v8, v33
	v_max_u32_e32 v33, v9, v6
	v_min_u32_e32 v6, v9, v6
	v_max_u32_e32 v9, v10, v7
	v_min_u32_e32 v7, v10, v7
	v_max_u32_e32 v10, v11, v19
	v_min_u32_e32 v11, v11, v19
	v_max_u32_e32 v19, v12, v21
	v_min_u32_e32 v12, v12, v21
	v_max_u32_e32 v21, v13, v29
	v_min_u32_e32 v13, v13, v29
	v_max_u32_e32 v29, v16, v23
	v_min_u32_e32 v16, v16, v23
	v_max_u32_e32 v40, v30, v39
	v_min_u32_e32 v30, v30, v39
	v_max_u32_e32 v39, v38, v32
	v_min_u32_e32 v32, v38, v32
	v_max_u32_e32 v38, v22, v14
	v_min_u32_e32 v14, v22, v14
	v_max_u32_e32 v22, v27, v15
	v_min_u32_e32 v15, v27, v15
	v_max_u32_e32 v27, v24, v20
	v_min_u32_e32 v20, v24, v20
	v_max_u32_e32 v24, v31, v18
	v_min_u32_e32 v18, v31, v18
	v_max_u32_e32 v31, v26, v34
	v_min_u32_e32 v26, v26, v34
	v_max_u32_e32 v34, v35, v28
	v_min_u32_e32 v28, v35, v28
	v_max_u32_e32 v23, v57, v10
	v_min_u32_e32 v10, v57, v10
	v_max_u32_e32 v57, v25, v19
	v_min_u32_e32 v19, v25, v19
	v_max_u32_e32 v25, v33, v21
	v_min_u32_e32 v21, v33, v21
	v_max_u32_e32 v33, v9, v29
	v_min_u32_e32 v9, v9, v29
	v_max_u32_e32 v29, v17, v11
	v_min_u32_e32 v11, v17, v11
	v_max_u32_e32 v17, v8, v12
	v_min_u32_e32 v8, v8, v12
	v_max_u32_e32 v12, v6, v13
	v_min_u32_e32 v6, v6, v13
	v_max_u32_e32 v13, v7, v16
	v_min_u32_e32 v7, v7, v16
	v_max_u32_e32 v35, v40, v27
	v_min_u32_e32 v27, v40, v27
	v_max_u32_e32 v40, v39, v24
	v_min_u32_e32 v24, v39, v24
	v_max_u32_e32 v39, v38, v31
	v_min_u32_e32 v31, v38, v31
	v_max_u32_e32 v38, v22, v34
	v_min_u32_e32 v22, v22, v34
	v_max_u32_e32 v34, v30, v20
	v_min_u32_e32 v20, v30, v20
	v_max_u32_e32 v30, v32, v18
	v_min_u32_e32 v18, v32, v18
	v_max_u32_e32 v32, v14, v26
	v_min_u32_e32 v14, v14, v26
	v_max_u32_e32 v26, v15, v28
	v_min_u32_e32 v15, v15, v28
	v_max_u32_e32 v16, v23, v25
	v_min_u32_e32 v25, v23, v25
	v_max_u32_e32 v58, v57, v33
	v_min_u32_e32 v33, v57, v33
	v_max_u32_e32 v57, v10, v21
	v_min_u32_e32 v10, v10, v21
	v_max_u32_e32 v59, v19, v9
	v_min_u32_e32 v9, v19, v9
	v_max_u32_e32 v60, v29, v12
	v_min_u32_e32 v61, v29, v12
	v_max_u32_e32 v12, v17, v13
	v_min_u32_e32 v62, v17, v13
	v_max_u32_e32 v63, v11, v6
	v_min_u32_e32 v64, v11, v6
	v_max_u32_e32 v65, v8, v7
	v_min_u32_e32 v66, v8, v7
	v_max_u32_e32 v41, v35, v39
	v_min_u32_e32 v35, v35, v39
	v_max_u32_e32 v39, v40, v38
	v_min_u32_e32 v38, v40, v38
	v_max_u32_e32 v40, v27, v31
	v_min_u32_e32 v27, v27, v31
	v_max_u32_e32 v31, v24, v22
	v_min_u32_e32 v22, v24, v22
	v_max_u32_e32 v24, v34, v32
	v_min_u32_e32 v42, v34, v32
	v_max_u32_e32 v43, v30, v26
	v_min_u32_e32 v30, v30, v26
	v_max_u32_e32 v47, v20, v14
	v_min_u32_e32 v48, v20, v14
	v_max_u32_e32 v49, v18, v15
	v_min_u32_e32 v50, v18, v15
	v_max_u32_e32 v23, v16, v58
	v_min_u32_e32 v29, v16, v58
	v_max_u32_e32 v21, v25, v33
	v_min_u32_e32 v19, v25, v33
	v_max_u32_e32 v7, v57, v59
	v_min_u32_e32 v6, v57, v59
	v_max_u32_e32 v33, v10, v9
	v_min_u32_e32 v17, v10, v9
	v_max_u32_e32 v16, v60, v12
	v_min_u32_e32 v13, v60, v12
	v_max_u32_e32 v12, v61, v62
	v_min_u32_e32 v11, v61, v62
	v_max_u32_e32 v10, v63, v65
	v_min_u32_e32 v9, v63, v65
	v_max_u32_e32 v8, v64, v66
	v_min_u32_e32 v25, v64, v66
	v_max_u32_e32 v28, v41, v39
	v_min_u32_e32 v34, v41, v39
	v_max_u32_e32 v18, v35, v38
	v_min_u32_e32 v20, v35, v38
	v_max_u32_e32 v15, v40, v31
	v_min_u32_e32 v14, v40, v31
	v_max_u32_e32 v32, v27, v22
	v_min_u32_e32 v74, v27, v22
	v_max_u32_e32 v35, v24, v43
	v_min_u32_e32 v26, v24, v43
	v_max_u32_e32 v31, v42, v30
	v_min_u32_e32 v24, v42, v30
	v_max_u32_e32 v27, v47, v49
	v_min_u32_e32 v22, v47, v49
	v_max_u32_e32 v73, v48, v50
	v_min_u32_e32 v30, v48, v50
